# final norm: expert rows gathered two per memory round trip (pair loop of layer-1 norm1 transplanted, same add order), acc copied once per row
# baseline (speedup 1.0000x reference)
; __device__ __forceinline__ f32x4 unpack_f8x4(unsigned w) { const auto lo = __builtin_amdgcn_cvt_pk_f32_fp8((int)w, false), hi = __builtin_amdgcn_cvt_pk_f32_fp8((int)w, true); return (f32x4){lo[0], lo[1], hi[0], hi[1]}; }
; __device__ __forceinline__ void gather_y1(const Ctx& F, const int s, f32x4 (&acc)[8]) {
; #pragma unroll
;     for (int j = 0; j < 8; ++j) acc[j] = (f32x4){0.f, 0.f, 0.f, 0.f};
; #pragma unroll 2
;     for (int e = 0; e < 16; ++e) { const int se = __builtin_amdgcn_readlane(s, e);
;         if (se >= 0) { const unsigned char* yr = F.y8 + (size_t)se * DM + 4 * F.lane;
; #pragma unroll
;             for (int j = 0; j < 8; ++j) { const unsigned w = __builtin_nontemporal_load((const unsigned*)(yr + 256 * j)); acc[j] += unpack_f8x4(w); } } }
; __device__ __forceinline__ void phase_norm1(const Params& p, const Ctx& F, const int l) {
;     ...
;         { const int t2 = t + tstride;
;           if (t2 < TPB) { const float* xs2; float* xd2; row_ptrs(p, F, l, b, t2, xs2, xd2);
; #pragma unroll
;             for (int j = 0; j < 8; ++j) vn[j] = __builtin_nontemporal_load((const f32x4*)xs2 + F.lane + 64 * j);
;             if (comb) {
; #pragma unroll
;                 for (int j = 0; j < 8; ++j) dn[j] = __builtin_nontemporal_load((const u32x2*)(F.dlt + ((size_t)b * TPB + t2) * DM + 4 * F.lane + 256 * j)); }
;             if (comb) { { if (fin) gather_y1(F, sn, accn); else gather_y(F, sn, accn); } const int t3 = t2 + tstride; sn = -1; if (t3 < TPB && F.lane < 16) sn = F.slot[(unsigned)((b * 16 + F.lane) * TPB + t3)]; } } }
.LBB0_1469:
	s_add_i32 s6, s26, s13
	s_cmpk_lt_i32 s6, 0x1100
	s_cselect_b64 s[24:25], -1, 0
	s_and_b64 s[24:25], s[24:25], s[0:1]
	v_add_u32_e32 v96, s6, v215
	v_cndmask_b32_e64 v96, 0, v96, s[24:25]
	v_mov_b32_e32 v97, v129
	v_lshl_add_u64 v[96:97], v[96:97], 2, s[2:3]
	global_load_dword v250, v[96:97], off
	s_lshl_b64 s[20:21], s[20:21], 13
	s_add_u32 s20, s22, s20
	s_addc_u32 s21, s23, s21
	v_lshl_add_u64 v[48:49], s[20:21], 0, v[128:129]
	global_load_dwordx4 v[32:35], v128, s[20:21] nt
	global_load_dwordx4 v[36:39], v128, s[20:21] offset:1024 nt
	global_load_dwordx4 v[40:43], v128, s[20:21] offset:2048 nt
	global_load_dwordx4 v[44:47], v128, s[20:21] offset:3072 nt
	s_add_u32 s20, s26, s28
	s_addc_u32 s21, s33, 0
	v_add_co_u32_e32 v60, vcc, s30, v48
	s_lshl_b64 s[20:21], s[20:21], 12
	s_nop 0
	v_addc_co_u32_e32 v61, vcc, 0, v49, vcc
	v_lshl_add_u64 v[96:97], v[190:191], 0, s[20:21]
	global_load_dwordx4 v[48:51], v[60:61], off nt
	global_load_dwordx4 v[52:55], v[60:61], off offset:1024 nt
	global_load_dwordx4 v[56:59], v[60:61], off offset:2048 nt
	s_nop 0
	global_load_dwordx4 v[60:63], v[60:61], off offset:3072 nt
	s_nop 0
	global_load_dwordx2 v[192:193], v[96:97], off nt
	global_load_dwordx2 v[194:195], v[96:97], off offset:512 nt
	global_load_dwordx2 v[196:197], v[96:97], off offset:1024 nt
	global_load_dwordx2 v[198:199], v[96:97], off offset:1536 nt
	global_load_dwordx2 v[200:201], v[96:97], off offset:2048 nt
	global_load_dwordx2 v[202:203], v[96:97], off offset:2560 nt
	global_load_dwordx2 v[204:205], v[96:97], off offset:3072 nt
	global_load_dwordx2 v[206:207], v[96:97], off offset:3584 nt
	v_mov_b32_e32 v98, v129
	v_mov_b32_e32 v99, v129
	v_mov_b32_e32 v96, v129
	v_mov_b32_e32 v97, v129
	v_mov_b64_e32 v[102:103], v[98:99]
	v_mov_b64_e32 v[106:107], v[98:99]
	v_mov_b64_e32 v[110:111], v[98:99]
	v_mov_b64_e32 v[114:115], v[98:99]
	v_mov_b64_e32 v[118:119], v[98:99]
	v_mov_b64_e32 v[122:123], v[98:99]
	v_mov_b64_e32 v[126:127], v[98:99]
	v_mov_b64_e32 v[100:101], v[96:97]
	v_mov_b64_e32 v[104:105], v[96:97]
	v_mov_b64_e32 v[108:109], v[96:97]
	v_mov_b64_e32 v[112:113], v[96:97]
	v_mov_b64_e32 v[116:117], v[96:97]
	v_mov_b64_e32 v[120:121], v[96:97]
	v_mov_b64_e32 v[124:125], v[96:97]
	v_cmp_lt_i32_e32 vcc, -1, v208
	s_and_b32 s40, vcc_lo, 0xffff
	s_cmp_eq_u32 s40, 0
	s_cbranch_scc1 .Lfp_done
; __device__ __forceinline__ f32x4 unpack_f8x4(unsigned w) { const auto lo = __builtin_amdgcn_cvt_pk_f32_fp8((int)w, false), hi = __builtin_amdgcn_cvt_pk_f32_fp8((int)w, true); return (f32x4){lo[0], lo[1], hi[0], hi[1]}; }
; __device__ __forceinline__ void gather_y(const Ctx& F, const int s, f32x4 (&acc)[8]) {
; #pragma unroll
;     for (int j = 0; j < 8; ++j) acc[j] = (f32x4){0.f, 0.f, 0.f, 0.f};
;     unsigned m = (unsigned)__ballot(s >= 0) & 0xffffu;
;     while (m) {
;         const int e0 = __builtin_ctz(m); m &= m - 1;
;         const bool two = m != 0; const int e1 = two ? __builtin_ctz(m) : e0; if (two) m &= m - 1;
;         const int s0 = __builtin_amdgcn_readlane(s, e0), s1 = __builtin_amdgcn_readlane(s, e1);
;         const unsigned char* y0 = F.y8 + (size_t)s0 * DM + 4 * F.lane; const unsigned char* y1 = F.y8 + (size_t)s1 * DM + 4 * F.lane;
;         unsigned w0[8], w1[8];
; #pragma unroll
;         for (int j = 0; j < 8; ++j) w0[j] = __builtin_nontemporal_load((const unsigned*)(y0 + 256 * j));
; #pragma unroll
;         for (int j = 0; j < 8; ++j) w1[j] = __builtin_nontemporal_load((const unsigned*)(y1 + 256 * j));
;         const float k1 = two ? 1.f : 0.f;
; #pragma unroll
;         for (int j = 0; j < 8; ++j) { acc[j] += unpack_f8x4(w0[j]); acc[j] += unpack_f8x4(w1[j]) * k1; }
;     }
; }
.Lfp_loop:
	s_add_i32 s41, s40, -1
	s_and_b32 s42, s41, s40
	s_ff1_i32_b32 s43, s40
	v_sub_co_u32_e64 v238, s[40:41], s42, 1
	s_ff1_i32_b32 s46, s42
	s_and_b64 s[44:45], s[40:41], exec
	s_cselect_b32 s45, s43, s46
	v_readlane_b32 s44, v208, s43
	v_readlane_b32 s46, v208, s45
	s_ashr_i32 s45, s44, 31
	s_lshl_b64 s[44:45], s[44:45], 11
	s_ashr_i32 s47, s46, 31
	v_lshl_add_u64 v[240:241], v[130:131], 0, s[44:45]
	s_lshl_b64 s[44:45], s[46:47], 11
	global_load_dword v217, v[240:241], off nt
	global_load_dword v218, v[240:241], off offset:256 nt
	global_load_dword v219, v[240:241], off offset:512 nt
	global_load_dword v220, v[240:241], off offset:768 nt
	global_load_dword v221, v[240:241], off offset:1024 nt
	global_load_dword v222, v[240:241], off offset:1280 nt
	global_load_dword v223, v[240:241], off offset:1536 nt
	global_load_dword v224, v[240:241], off offset:1792 nt
	v_lshl_add_u64 v[240:241], v[130:131], 0, s[44:45]
	global_load_dword v225, v[240:241], off nt
	global_load_dword v226, v[240:241], off offset:256 nt
	global_load_dword v227, v[240:241], off offset:512 nt
	global_load_dword v228, v[240:241], off offset:768 nt
	global_load_dword v229, v[240:241], off offset:1024 nt
	global_load_dword v230, v[240:241], off offset:1280 nt
	global_load_dword v231, v[240:241], off offset:1536 nt
	s_nop 0
	global_load_dword v241, v[240:241], off offset:1792 nt
	v_cndmask_b32_e64 v240, 1.0, 0, s[40:41]
	v_readfirstlane_b32 s40, v238
	s_and_b32 s40, s40, s42
	s_cmp_lg_u32 s40, 0
	s_waitcnt vmcnt(15)
	v_cvt_pk_f32_fp8_e32 v[234:235], v217
	v_cvt_pk_f32_fp8_sdwa v[236:237], v217 src0_sel:WORD_1
	v_pk_add_f32 v[124:125], v[124:125], v[234:235]
	v_pk_add_f32 v[126:127], v[126:127], v[236:237]
	s_waitcnt vmcnt(7)
	v_cvt_pk_f32_fp8_e32 v[234:235], v225
	v_cvt_pk_f32_fp8_sdwa v[236:237], v225 src0_sel:WORD_1
	s_waitcnt vmcnt(0)
	v_pk_fma_f32 v[124:125], v[240:241], v[234:235], v[124:125] op_sel_hi:[0,1,1]
	v_pk_fma_f32 v[126:127], v[240:241], v[236:237], v[126:127] op_sel_hi:[0,1,1]
	v_cvt_pk_f32_fp8_e32 v[234:235], v218
	v_cvt_pk_f32_fp8_sdwa v[236:237], v218 src0_sel:WORD_1
	v_pk_add_f32 v[120:121], v[120:121], v[234:235]
	v_pk_add_f32 v[122:123], v[122:123], v[236:237]
	v_cvt_pk_f32_fp8_e32 v[234:235], v226
	v_cvt_pk_f32_fp8_sdwa v[236:237], v226 src0_sel:WORD_1
	v_pk_fma_f32 v[120:121], v[240:241], v[234:235], v[120:121] op_sel_hi:[0,1,1]
	v_pk_fma_f32 v[122:123], v[240:241], v[236:237], v[122:123] op_sel_hi:[0,1,1]
	v_cvt_pk_f32_fp8_e32 v[234:235], v219
	v_cvt_pk_f32_fp8_sdwa v[236:237], v219 src0_sel:WORD_1
	v_pk_add_f32 v[116:117], v[116:117], v[234:235]
	v_pk_add_f32 v[118:119], v[118:119], v[236:237]
	v_cvt_pk_f32_fp8_e32 v[234:235], v227
	v_cvt_pk_f32_fp8_sdwa v[236:237], v227 src0_sel:WORD_1
	v_pk_fma_f32 v[116:117], v[240:241], v[234:235], v[116:117] op_sel_hi:[0,1,1]
	v_pk_fma_f32 v[118:119], v[240:241], v[236:237], v[118:119] op_sel_hi:[0,1,1]
	v_cvt_pk_f32_fp8_e32 v[234:235], v220
	v_cvt_pk_f32_fp8_sdwa v[236:237], v220 src0_sel:WORD_1
	v_pk_add_f32 v[112:113], v[112:113], v[234:235]
	v_pk_add_f32 v[114:115], v[114:115], v[236:237]
	v_cvt_pk_f32_fp8_e32 v[234:235], v228
	v_cvt_pk_f32_fp8_sdwa v[236:237], v228 src0_sel:WORD_1
	v_pk_fma_f32 v[112:113], v[240:241], v[234:235], v[112:113] op_sel_hi:[0,1,1]
	v_pk_fma_f32 v[114:115], v[240:241], v[236:237], v[114:115] op_sel_hi:[0,1,1]
	v_cvt_pk_f32_fp8_e32 v[234:235], v221
	v_cvt_pk_f32_fp8_sdwa v[236:237], v221 src0_sel:WORD_1
	v_pk_add_f32 v[108:109], v[108:109], v[234:235]
	v_pk_add_f32 v[110:111], v[110:111], v[236:237]
	v_cvt_pk_f32_fp8_e32 v[234:235], v229
	v_cvt_pk_f32_fp8_sdwa v[236:237], v229 src0_sel:WORD_1
	v_pk_fma_f32 v[108:109], v[240:241], v[234:235], v[108:109] op_sel_hi:[0,1,1]
	v_pk_fma_f32 v[110:111], v[240:241], v[236:237], v[110:111] op_sel_hi:[0,1,1]
	v_cvt_pk_f32_fp8_e32 v[234:235], v222
	v_cvt_pk_f32_fp8_sdwa v[236:237], v222 src0_sel:WORD_1
	v_pk_add_f32 v[104:105], v[104:105], v[234:235]
	v_pk_add_f32 v[106:107], v[106:107], v[236:237]
	v_cvt_pk_f32_fp8_e32 v[234:235], v230
	v_cvt_pk_f32_fp8_sdwa v[236:237], v230 src0_sel:WORD_1
	v_pk_fma_f32 v[104:105], v[240:241], v[234:235], v[104:105] op_sel_hi:[0,1,1]
	v_pk_fma_f32 v[106:107], v[240:241], v[236:237], v[106:107] op_sel_hi:[0,1,1]
	v_cvt_pk_f32_fp8_e32 v[234:235], v223
	v_cvt_pk_f32_fp8_sdwa v[236:237], v223 src0_sel:WORD_1
	v_pk_add_f32 v[100:101], v[100:101], v[234:235]
	v_pk_add_f32 v[102:103], v[102:103], v[236:237]
	v_cvt_pk_f32_fp8_e32 v[234:235], v231
	v_cvt_pk_f32_fp8_sdwa v[236:237], v231 src0_sel:WORD_1
	v_pk_fma_f32 v[100:101], v[240:241], v[234:235], v[100:101] op_sel_hi:[0,1,1]
	v_pk_fma_f32 v[102:103], v[240:241], v[236:237], v[102:103] op_sel_hi:[0,1,1]
	v_cvt_pk_f32_fp8_e32 v[234:235], v224
	v_cvt_pk_f32_fp8_sdwa v[236:237], v224 src0_sel:WORD_1
	v_pk_add_f32 v[96:97], v[96:97], v[234:235]
	v_pk_add_f32 v[98:99], v[98:99], v[236:237]
	v_cvt_pk_f32_fp8_e32 v[234:235], v241
	v_cvt_pk_f32_fp8_sdwa v[236:237], v241 src0_sel:WORD_1
	v_pk_fma_f32 v[96:97], v[240:241], v[234:235], v[96:97] op_sel_hi:[0,1,1]
	v_pk_fma_f32 v[98:99], v[240:241], v[236:237], v[98:99] op_sel_hi:[0,1,1]
	s_cbranch_scc1 .Lfp_loop
.Lfp_done:
	v_mov_b32_e32 v217, v124
	v_mov_b32_e32 v218, v125
	v_mov_b32_e32 v219, v126
	v_mov_b32_e32 v220, v127
	v_mov_b32_e32 v221, v120
	v_mov_b32_e32 v222, v121
	v_mov_b32_e32 v223, v122
	v_mov_b32_e32 v224, v123
	v_mov_b32_e32 v225, v116
	v_mov_b32_e32 v226, v117
	v_mov_b32_e32 v227, v118
	v_mov_b32_e32 v228, v119
	v_mov_b32_e32 v229, v112
	v_mov_b32_e32 v230, v113
	v_mov_b32_e32 v231, v114
	v_mov_b32_e32 v232, v115
	v_mov_b32_e32 v233, v108
	v_mov_b32_e32 v235, v109
	v_mov_b32_e32 v236, v110
	v_mov_b32_e32 v237, v111
	v_mov_b32_e32 v238, v104
	v_mov_b32_e32 v239, v105
	v_mov_b32_e32 v240, v106
	v_mov_b32_e32 v241, v107
	v_mov_b32_e32 v242, v100
	v_mov_b32_e32 v243, v101
	v_mov_b32_e32 v244, v102
	v_mov_b32_e32 v245, v103
	v_mov_b32_e32 v246, v96
	v_mov_b32_e32 v247, v97
	v_mov_b32_e32 v248, v98
	v_mov_b32_e32 v234, v99
	s_branch .LBB0_1459
